# scheduling: weight-conversion slot between attention units chosen per XCD so an XCD's workgroups stay in step on their shared K/V tiles
# baseline (speedup 1.0000x reference)
.LBB0_980:
	v_readlane_b32 s8, v255, 45
	s_bfe_u32 s8, s8, 0x20005
	s_cmp_eq_u32 s74, s8
	s_cselect_b64 s[8:9], -1, 0
	s_and_b64 s[8:9], s[14:15], s[8:9]
	s_andn2_b64 vcc, exec, s[8:9]
	s_cbranch_vccnz .LBB0_1053
	s_barrier
	v_mbcnt_lo_u32_b32 v66, -1, 0
	v_mbcnt_hi_u32_b32 v66, -1, v66
	s_getreg_b32 s8, hwreg(HW_REG_HW_ID, 0, 6)
	s_lshl_b32 s8, s8, 2
	s_and_b32 s8, s8, 0xfc
	s_or_b32 s8, s8, 0x27100
	v_mov_b32_e32 v0, s8
	ds_read_b32 v0, v0
	s_mov_b64 s[10:11], -1
	s_and_b64 vcc, exec, s[16:17]
	s_waitcnt lgkmcnt(0)
	v_readfirstlane_b32 s13, v0
	s_cbranch_vccz .LBB0_983
	s_mov_b32 s8, 31
	s_ashr_i32 s9, s8, 31
	s_lshl_b64 s[8:9], s[8:9], 3
	s_add_u32 s8, s0, s8
	s_addc_u32 s9, s1, s9
	s_load_dwordx2 s[8:9], s[8:9], 0x0
	s_lshl_b64 s[10:11], s[18:19], 2
	s_mov_b32 s12, 35
	s_waitcnt lgkmcnt(0)
	s_add_u32 s8, s8, s10
	s_addc_u32 s9, s9, s11
	s_mov_b64 s[10:11], 0
